# speedup vs baseline: 1.1349x; 1.1349x over previous
.LBB1_36:
	s_or_b64 exec, exec, s[2:3]
	s_mul_i32 s2, s24, 0x500
	v_or_b32_e32 v68, s2, v101
	v_mov_b32_e32 v69, 0
	s_add_i32 s3, s2, 0x100
	v_lshl_add_u64 v[66:67], v[68:69], 2, s[6:7]
	v_or_b32_e32 v64, s3, v101
	v_mov_b32_e32 v65, v69
	s_add_i32 s3, s2, 0x140
	global_load_dword v103, v[66:67], off
	global_load_dword v108, v[66:67], off offset:256
	global_load_dword v109, v[66:67], off offset:512
	global_load_dword v110, v[66:67], off offset:768
	v_lshl_add_u64 v[72:73], v[64:65], 2, s[6:7]
	v_or_b32_e32 v64, s3, v101
	s_add_i32 s3, s2, 0x180
	global_load_dword v111, v[72:73], off
	v_lshl_add_u64 v[64:65], v[64:65], 2, s[6:7]
	v_or_b32_e32 v70, s3, v101
	v_mov_b32_e32 v71, v69
	global_load_dword v112, v[64:65], off
	v_lshl_add_u64 v[70:71], v[70:71], 2, s[6:7]
	global_load_dword v113, v[70:71], off
	s_add_i32 s3, s2, 0x1c0
	v_mov_b32_e32 v75, v69
	s_add_i32 s4, s2, 0x200
	s_add_i32 s5, s2, 0x240
	s_add_i32 s11, s2, 0x280
	v_or_b32_e32 v74, s3, v101
	v_mov_b32_e32 v77, v69
	v_mov_b32_e32 v79, v69
	v_mov_b32_e32 v81, v69
	v_or_b32_e32 v76, s4, v101
	v_or_b32_e32 v78, s5, v101
	v_or_b32_e32 v80, s11, v101
	v_lshl_add_u64 v[90:91], v[74:75], 2, s[6:7]
	v_lshl_add_u64 v[88:89], v[76:77], 2, s[6:7]
	v_lshl_add_u64 v[82:83], v[78:79], 2, s[6:7]
	v_lshl_add_u64 v[80:81], v[80:81], 2, s[6:7]
	global_load_dword v114, v[90:91], off
	global_load_dword v115, v[88:89], off
	global_load_dword v116, v[82:83], off
	global_load_dword v117, v[80:81], off
	s_add_i32 s15, s2, 0x300
	s_add_i32 s3, s2, 0x3c0
	v_mov_b32_e32 v87, v69
	v_or_b32_e32 v86, s15, v101
	v_or_b32_e32 v74, s3, v101
	v_lshl_add_u64 v[96:97], v[86:87], 2, s[6:7]
	v_lshl_add_u64 v[86:87], v[74:75], 2, s[6:7]
	s_add_i32 s16, s2, 0x340
	s_add_i32 s17, s2, 0x380
	v_mov_b32_e32 v93, v69
	v_mov_b32_e32 v105, v69
	v_or_b32_e32 v92, s16, v101
	v_or_b32_e32 v104, s17, v101
	v_lshl_add_u64 v[94:95], v[92:93], 2, s[6:7]
	v_lshl_add_u64 v[92:93], v[104:105], 2, s[6:7]
	s_add_i32 s14, s2, 0x2c0
	v_mov_b32_e32 v85, v69
	s_add_i32 s4, s2, 0x400
	v_or_b32_e32 v84, s14, v101
	s_add_i32 s5, s2, 0x440
	s_add_i32 s11, s2, 0x480
	v_or_b32_e32 v76, s4, v101
	v_lshl_add_u64 v[98:99], v[84:85], 2, s[6:7]
	v_mov_b32_e32 v107, v69
	v_or_b32_e32 v78, s5, v101
	v_or_b32_e32 v106, s11, v101
	v_lshl_add_u64 v[84:85], v[76:77], 2, s[6:7]
	global_load_dword v118, v[98:99], off
	global_load_dword v119, v[96:97], off
	global_load_dword v120, v[94:95], off
	global_load_dword v121, v[92:93], off
	global_load_dword v122, v[86:87], off
	v_lshl_add_u64 v[78:79], v[78:79], 2, s[6:7]
	v_lshl_add_u64 v[76:77], v[106:107], 2, s[6:7]
	s_addk_i32 s2, 0x4c0
	s_mov_b32 s14, 0xf800000
	s_mov_b32 s11, 0x41e6d4ca
	s_waitcnt vmcnt(15)
	v_add_f32_e32 v74, 0, v103
	s_waitcnt vmcnt(14)
	v_add_f32_e32 v74, v74, v108
	s_waitcnt vmcnt(13)
	v_add_f32_e32 v74, v74, v109
	s_waitcnt vmcnt(12)
	v_add_f32_e32 v74, v74, v110
	global_load_dword v103, v[84:85], off
	global_load_dword v109, v[76:77], off
	s_waitcnt vmcnt(13)
	v_add_f32_e32 v74, v74, v111
	s_waitcnt vmcnt(12)
	v_add_f32_e32 v74, v74, v112
	global_load_dword v112, v[66:67], off offset:64
	s_waitcnt vmcnt(12)
	v_add_f32_e32 v104, v74, v113
	v_or_b32_e32 v74, s2, v101
	v_lshl_add_u64 v[74:75], v[74:75], 2, s[6:7]
	global_load_dword v110, v[74:75], off
	s_waitcnt vmcnt(12)
	v_add_f32_e32 v104, v104, v114
	s_waitcnt vmcnt(11)
	v_add_f32_e32 v104, v104, v115
	s_waitcnt vmcnt(10)
	v_add_f32_e32 v104, v104, v116
	s_waitcnt vmcnt(9)
	v_add_f32_e32 v111, v104, v117
	v_or_b32_e32 v104, 16, v68
	v_lshl_add_u64 v[106:107], v[104:105], 2, s[6:7]
	global_load_dword v113, v[106:107], off offset:256
	global_load_dword v108, v[78:79], off
	s_waitcnt vmcnt(10)
	v_add_f32_e32 v104, v111, v118
	s_waitcnt vmcnt(9)
	v_add_f32_e32 v104, v104, v119
	s_waitcnt vmcnt(8)
	v_add_f32_e32 v104, v104, v120
	s_waitcnt vmcnt(7)
	v_add_f32_e32 v104, v104, v121
	s_waitcnt vmcnt(6)
	v_add_f32_e32 v104, v104, v122
	s_waitcnt vmcnt(5)
	v_add_f32_e32 v103, v104, v103
	s_waitcnt vmcnt(3)
	v_add_f32_e32 v112, 0, v112
	s_waitcnt vmcnt(1)
	v_add_f32_e32 v112, v112, v113
	s_waitcnt vmcnt(0)
	v_add_f32_e32 v103, v103, v108
	v_add_f32_e32 v103, v103, v109
	v_add_f32_e32 v103, v103, v110
	v_cmp_gt_f32_e32 vcc, s14, v103
	v_mul_f32_e32 v104, 0x4f800000, v103
	s_nop 0
	v_cndmask_b32_e32 v104, v103, v104, vcc
	v_sqrt_f32_e32 v103, v104
	s_nop 0
	v_add_u32_e32 v105, -1, v103
	v_fma_f32 v108, -v105, v103, v104
	v_cmp_ge_f32_e64 s[2:3], 0, v108
	v_add_u32_e32 v108, 1, v103
	s_nop 0
	v_cndmask_b32_e64 v105, v103, v105, s[2:3]
	v_fma_f32 v103, -v108, v103, v104
	v_cmp_lt_f32_e64 s[2:3], 0, v103
	s_nop 1
	v_cndmask_b32_e64 v103, v105, v108, s[2:3]
	v_mul_f32_e32 v105, 0x37800000, v103
	v_cndmask_b32_e32 v105, v103, v105, vcc
	v_mov_b32_e32 v103, 0x260
	v_cmp_class_f32_e32 vcc, v104, v103
	s_nop 1
	v_cndmask_b32_e32 v104, v105, v104, vcc
	v_add_f32_e32 v104, 0x322bcc77, v104
	v_div_scale_f32 v108, s[2:3], v104, v104, s11
	v_rcp_f32_e32 v105, v108
	s_nop 0
	v_fma_f32 v109, -v108, v105, 1.0
	v_fmac_f32_e32 v105, v109, v105
	global_load_dword v109, v[106:107], off offset:512
	s_nop 0
	global_load_dword v106, v[106:107], off offset:768
	s_nop 0
	global_load_dword v107, v[72:73], off offset:64
	global_load_dword v110, v[64:65], off offset:64
	global_load_dword v111, v[70:71], off offset:64
	global_load_dword v114, v[90:91], off offset:64
	global_load_dword v115, v[88:89], off offset:64
	global_load_dword v116, v[82:83], off offset:64
	global_load_dword v113, v[80:81], off offset:64
	s_waitcnt vmcnt(8)
	v_add_f32_e32 v109, v112, v109
	s_waitcnt vmcnt(7)
	v_add_f32_e32 v106, v109, v106
	s_waitcnt vmcnt(6)
	v_add_f32_e32 v106, v106, v107
	global_load_dword v107, v[98:99], off offset:64
	global_load_dword v109, v[96:97], off offset:64
	s_waitcnt vmcnt(7)
	v_add_f32_e32 v106, v106, v110
	s_waitcnt vmcnt(6)
	v_add_f32_e32 v106, v106, v111
	s_waitcnt vmcnt(5)
	v_add_f32_e32 v106, v106, v114
	s_waitcnt vmcnt(4)
	v_add_f32_e32 v106, v106, v115
	s_waitcnt vmcnt(3)
	v_add_f32_e32 v106, v106, v116
	s_waitcnt vmcnt(2)
	v_add_f32_e32 v106, v106, v113
	global_load_dword v110, v[94:95], off offset:64
	global_load_dword v111, v[92:93], off offset:64
	global_load_dword v112, v[86:87], off offset:64
	global_load_dword v113, v[84:85], off offset:64
	global_load_dword v114, v[78:79], off offset:64
	global_load_dword v115, v[76:77], off offset:64
	global_load_dword v116, v[74:75], off offset:64
	s_waitcnt vmcnt(8)
	v_add_f32_e32 v106, v106, v107
	s_waitcnt vmcnt(7)
	v_add_f32_e32 v109, v106, v109
	s_waitcnt vmcnt(6)
	v_add_f32_e32 v109, v109, v110
	s_waitcnt vmcnt(5)
	v_add_f32_e32 v109, v109, v111
	s_waitcnt vmcnt(4)
	v_add_f32_e32 v109, v109, v112
	s_waitcnt vmcnt(3)
	v_add_f32_e32 v109, v109, v113
	s_waitcnt vmcnt(2)
	v_add_f32_e32 v109, v109, v114
	s_waitcnt vmcnt(1)
	v_add_f32_e32 v109, v109, v115
	s_waitcnt vmcnt(0)
	v_add_f32_e32 v109, v109, v116
	v_cmp_gt_f32_e64 s[2:3], s14, v109
	v_mul_f32_e32 v110, 0x4f800000, v109
	v_div_scale_f32 v107, vcc, s11, v104, s11
	v_cndmask_b32_e64 v109, v109, v110, s[2:3]
	v_sqrt_f32_e32 v110, v109
	v_mul_f32_e32 v106, v107, v105
	v_fma_f32 v111, -v108, v106, v107
	v_fmac_f32_e32 v106, v111, v105
	v_fma_f32 v107, -v108, v106, v107
	v_add_u32_e32 v108, -1, v110
	v_fma_f32 v111, -v108, v110, v109
	v_cmp_ge_f32_e64 s[4:5], 0, v111
	v_add_u32_e32 v111, 1, v110
	s_nop 0
	v_cndmask_b32_e64 v108, v110, v108, s[4:5]
	v_fma_f32 v110, -v111, v110, v109
	v_cmp_lt_f32_e64 s[4:5], 0, v110
	s_nop 1
	v_cndmask_b32_e64 v108, v108, v111, s[4:5]
	v_mul_f32_e32 v110, 0x37800000, v108
	v_cndmask_b32_e64 v108, v108, v110, s[2:3]
	v_cmp_class_f32_e64 s[2:3], v109, v103
	v_or_b32_e32 v110, 32, v68
	v_mov_b32_e32 v111, v69
	v_cndmask_b32_e64 v108, v108, v109, s[2:3]
	global_load_dword v109, v[66:67], off offset:128
	v_lshl_add_u64 v[112:113], v[110:111], 2, s[6:7]
	global_load_dword v110, v[112:113], off offset:256
	global_load_dword v111, v[112:113], off offset:512
	s_nop 0
	global_load_dword v112, v[112:113], off offset:768
	s_nop 0
	global_load_dword v113, v[72:73], off offset:128
	global_load_dword v114, v[66:67], off offset:192
	v_or_b32_e32 v68, 48, v68
	v_lshl_add_u64 v[66:67], v[68:69], 2, s[6:7]
	global_load_dword v68, v[66:67], off offset:256
	global_load_dword v115, v[66:67], off offset:512
	s_nop 0
	global_load_dword v66, v[66:67], off offset:768
	s_nop 0
	global_load_dword v67, v[64:65], off offset:128
	s_nop 0
	global_load_dword v72, v[72:73], off offset:192
	s_nop 0
	global_load_dword v73, v[70:71], off offset:128
	global_load_dword v116, v[64:65], off offset:192
	s_nop 0
	global_load_dword v65, v[90:91], off offset:128
	s_nop 0
	global_load_dword v70, v[70:71], off offset:192
	s_nop 0
	global_load_dword v71, v[88:89], off offset:128
	s_nop 0
	global_load_dword v90, v[90:91], off offset:192
	s_nop 0
	global_load_dword v91, v[82:83], off offset:128
	s_nop 0
	global_load_dword v88, v[88:89], off offset:192
	s_nop 0
	global_load_dword v89, v[80:81], off offset:128
	s_nop 0
	global_load_dword v82, v[82:83], off offset:192
	s_nop 0
	global_load_dword v83, v[98:99], off offset:128
	s_nop 0
	global_load_dword v80, v[80:81], off offset:192
	s_nop 0
	global_load_dword v81, v[96:97], off offset:128
	s_nop 0
	global_load_dword v98, v[98:99], off offset:192
	s_nop 0
	global_load_dword v99, v[94:95], off offset:128
	s_nop 0
	global_load_dword v96, v[96:97], off offset:192
	s_nop 0
	global_load_dword v97, v[92:93], off offset:128
	s_nop 0
	global_load_dword v94, v[94:95], off offset:192
	s_nop 0
	global_load_dword v95, v[86:87], off offset:128
	s_nop 0
	global_load_dword v92, v[92:93], off offset:192
	s_nop 0
	global_load_dword v93, v[84:85], off offset:128
	s_nop 0
	global_load_dword v86, v[86:87], off offset:192
	s_nop 0
	global_load_dword v87, v[78:79], off offset:128
	s_nop 0
	global_load_dword v84, v[84:85], off offset:192
	s_nop 0
	global_load_dword v85, v[76:77], off offset:128
	s_nop 0
	global_load_dword v78, v[78:79], off offset:192
	s_nop 0
	global_load_dword v79, v[74:75], off offset:128
	v_div_fmas_f32 v64, v107, v105, v106
	global_load_dword v76, v[76:77], off offset:192
	s_mul_i32 s2, s23, 0x1f80
	global_load_dword v74, v[74:75], off offset:192
	v_add_f32_e32 v108, 0x322bcc77, v108
	s_add_i32 s6, s8, s2
	v_div_scale_f32 v77, s[2:3], v108, v108, s11
	v_rcp_f32_e32 v117, v77
	v_div_fixup_f32 v64, v64, v104, s11
	v_lshrrev_b32_e32 v75, 4, v100
	v_fma_f32 v104, -v77, v117, 1.0
	v_fmac_f32_e32 v117, v104, v117
	v_div_scale_f32 v104, vcc, s11, v108, s11
	v_mul_f32_e32 v105, v104, v117
	s_waitcnt vmcnt(39)
	v_add_f32_e32 v106, 0, v109
	s_waitcnt vmcnt(38)
	v_add_f32_e32 v106, v106, v110
	s_waitcnt vmcnt(37)
	v_add_f32_e32 v106, v106, v111
	s_waitcnt vmcnt(36)
	v_add_f32_e32 v106, v106, v112
	s_waitcnt vmcnt(35)
	v_add_f32_e32 v106, v106, v113
	s_waitcnt vmcnt(30)
	v_add_f32_e32 v67, v106, v67
	s_waitcnt vmcnt(28)
	v_add_f32_e32 v67, v67, v73
	s_waitcnt vmcnt(26)
	v_add_f32_e32 v65, v67, v65
	s_waitcnt vmcnt(24)
	v_add_f32_e32 v65, v65, v71
	s_waitcnt vmcnt(22)
	v_add_f32_e32 v65, v65, v91
	s_waitcnt vmcnt(20)
	v_add_f32_e32 v65, v65, v89
	s_waitcnt vmcnt(18)
	v_add_f32_e32 v65, v65, v83
	s_waitcnt vmcnt(16)
	v_add_f32_e32 v65, v65, v81
	s_waitcnt vmcnt(14)
	v_add_f32_e32 v65, v65, v99
	s_waitcnt vmcnt(12)
	v_add_f32_e32 v65, v65, v97
	s_waitcnt vmcnt(10)
	v_add_f32_e32 v65, v65, v95
	s_waitcnt vmcnt(8)
	v_add_f32_e32 v65, v65, v93
	s_waitcnt vmcnt(6)
	v_add_f32_e32 v65, v65, v87
	s_waitcnt vmcnt(4)
	v_add_f32_e32 v65, v65, v85
	s_waitcnt vmcnt(2)
	v_add_f32_e32 v65, v65, v79
	v_cmp_gt_f32_e64 s[2:3], s14, v65
	v_mul_f32_e32 v67, 0x4f800000, v65
	v_add_f32_e32 v81, 0, v114
	v_cndmask_b32_e64 v65, v65, v67, s[2:3]
	v_add_f32_e32 v68, v81, v68
	v_sqrt_f32_e32 v67, v65
	v_add_f32_e32 v68, v68, v115
	v_add_f32_e32 v66, v68, v66
	v_add_f32_e32 v66, v66, v72
	v_fma_f32 v71, -v77, v105, v104
	v_add_f32_e32 v66, v66, v116
	v_fmac_f32_e32 v105, v71, v117
	v_add_u32_e32 v73, -1, v67
	v_add_f32_e32 v66, v66, v70
	v_fma_f32 v71, -v77, v105, v104
	v_fma_f32 v77, -v73, v67, v65
	v_add_f32_e32 v66, v66, v90
	v_cmp_ge_f32_e64 s[4:5], 0, v77
	v_add_u32_e32 v77, 1, v67
	v_add_f32_e32 v66, v66, v88
	v_cndmask_b32_e64 v73, v67, v73, s[4:5]
	v_fma_f32 v67, -v77, v67, v65
	v_add_f32_e32 v66, v66, v82
	v_cmp_lt_f32_e64 s[4:5], 0, v67
	v_add_f32_e32 v66, v66, v80
	v_add_f32_e32 v66, v66, v98
	v_cndmask_b32_e64 v67, v73, v77, s[4:5]
	v_mul_f32_e32 v73, 0x37800000, v67
	v_add_f32_e32 v66, v66, v96
	v_cndmask_b32_e64 v67, v67, v73, s[2:3]
	v_cmp_class_f32_e64 s[2:3], v65, v103
	v_add_f32_e32 v66, v66, v94
	v_add_f32_e32 v66, v66, v92
	v_cndmask_b32_e64 v65, v67, v65, s[2:3]
	v_add_f32_e32 v67, 0x322bcc77, v65
	v_add_f32_e32 v66, v66, v86
	v_div_scale_f32 v73, s[2:3], v67, v67, s11
	v_add_f32_e32 v66, v66, v84
	v_rcp_f32_e32 v77, v73
	v_add_f32_e32 v66, v66, v78
	s_waitcnt vmcnt(1)
	v_add_f32_e32 v66, v66, v76
	s_waitcnt vmcnt(0)
	v_add_f32_e32 v66, v66, v74
	v_cmp_gt_f32_e64 s[2:3], s14, v66
	v_mul_f32_e32 v68, 0x4f800000, v66
	v_div_fmas_f32 v65, v71, v117, v105
	v_fma_f32 v71, -v73, v77, 1.0
	v_cndmask_b32_e64 v66, v66, v68, s[2:3]
	v_fmac_f32_e32 v77, v71, v77
	v_div_scale_f32 v71, vcc, s11, v67, s11
	v_sqrt_f32_e32 v68, v66
	v_mul_f32_e32 v79, v71, v77
	v_fma_f32 v70, -v73, v79, v71
	v_fmac_f32_e32 v79, v70, v77
	v_fma_f32 v70, -v73, v79, v71
	v_add_u32_e32 v71, -1, v68
	v_fma_f32 v72, -v71, v68, v66
	v_cmp_ge_f32_e64 s[4:5], 0, v72
	v_add_u32_e32 v72, 1, v68
	v_div_fixup_f32 v65, v65, v108, s11
	v_cndmask_b32_e64 v71, v68, v71, s[4:5]
	v_fma_f32 v68, -v72, v68, v66
	v_cmp_lt_f32_e64 s[4:5], 0, v68
	s_nop 1
	v_cndmask_b32_e64 v68, v71, v72, s[4:5]
	v_mul_f32_e32 v71, 0x37800000, v68
	v_cndmask_b32_e64 v68, v68, v71, s[2:3]
	v_cmp_class_f32_e64 s[2:3], v66, v103
	s_nop 1
	v_cndmask_b32_e64 v66, v68, v66, s[2:3]
	v_add_f32_e32 v72, 0x322bcc77, v66
	v_div_scale_f32 v66, s[2:3], v72, v72, s11
	v_rcp_f32_e32 v73, v66
	v_div_fmas_f32 v68, v70, v77, v79
	v_div_fixup_f32 v68, v68, v67, s11
	s_movk_i32 s2, 0x88
	v_fma_f32 v67, -v66, v73, 1.0
	v_fmac_f32_e32 v73, v67, v73
	v_div_scale_f32 v67, vcc, s11, v72, s11
	v_mul_f32_e32 v70, v67, v73
	v_fma_f32 v71, -v66, v70, v67
	v_fmac_f32_e32 v70, v71, v73
	v_fma_f32 v67, -v66, v70, v67
	v_and_b32_e32 v66, 0x70, v100
	v_add_u32_e32 v71, s10, v66
	ds_read_b128 v[76:79], v71 offset:8832
	v_div_fmas_f32 v67, v67, v73, v70
	v_div_fixup_f32 v70, v67, v72, s11
	v_lshlrev_b32_e32 v67, 3, v75
	v_add_u32_e32 v72, s6, v67
	s_waitcnt lgkmcnt(0)
	v_mul_f32_e32 v73, v76, v64
	v_fmaak_f32 v60, v60, v73, 0xc1e6d4ca
	v_exp_f32_e32 v73, v60
	v_mul_f32_e32 v60, v77, v64
	v_fmaak_f32 v60, v61, v60, 0xc1e6d4ca
	v_mul_f32_e32 v61, v78, v64
	v_fmaak_f32 v61, v62, v61, 0xc1e6d4ca
	v_mul_f32_e32 v62, v79, v64
	v_fmaak_f32 v62, v63, v62, 0xc1e6d4ca
	v_exp_f32_e32 v61, v61
	v_exp_f32_e32 v62, v62
	v_exp_f32_e32 v74, v60
	v_mad_u32_u24 v60, v101, s2, v72
	s_mov_b32 s10, s9
	v_cvt_pk_bf16_f32 v63, v61, v62
	v_mul_f32_e32 v61, v76, v65
	v_fmaak_f32 v56, v56, v61, 0xc1e6d4ca
	v_mul_f32_e32 v61, v77, v65
	v_fmaak_f32 v57, v57, v61, 0xc1e6d4ca
	v_exp_f32_e32 v61, v57
	v_mul_f32_e32 v57, v78, v65
	v_cvt_pk_bf16_f32 v62, v73, v74
	v_fmaak_f32 v57, v58, v57, 0xc1e6d4ca
	ds_write_b64 v60, v[62:63] offset:10240
	v_exp_f32_e32 v62, v57
	v_mul_f32_e32 v57, v79, v65
	v_fmaak_f32 v57, v59, v57, 0xc1e6d4ca
	v_exp_f32_e32 v56, v56
	v_exp_f32_e32 v59, v57
	v_mov_b32_e32 v57, 0x880
	v_mad_u32_u24 v57, v101, s2, v57
	v_add_u32_e32 v58, v72, v57
	v_cvt_pk_bf16_f32 v63, v62, v59
	v_cvt_pk_bf16_f32 v62, v56, v61
	v_mul_f32_e32 v56, v76, v68
	v_fmaak_f32 v52, v52, v56, 0xc1e6d4ca
	v_exp_f32_e32 v56, v52
	v_mul_f32_e32 v52, v77, v68
	v_fmaak_f32 v52, v53, v52, 0xc1e6d4ca
	v_exp_f32_e32 v59, v52
	v_mul_f32_e32 v52, v78, v68
	v_fmaak_f32 v52, v54, v52, 0xc1e6d4ca
	v_exp_f32_e32 v54, v52
	v_mul_f32_e32 v52, v79, v68
	v_fmaak_f32 v52, v55, v52, 0xc1e6d4ca
	v_exp_f32_e32 v55, v52
	v_mov_b32_e32 v52, 0x1100
	v_mad_u32_u24 v52, v101, s2, v52
	v_add_u32_e32 v53, v72, v52
	v_cvt_pk_bf16_f32 v55, v54, v55
	v_cvt_pk_bf16_f32 v54, v56, v59
	ds_write_b64 v53, v[54:55] offset:10240
	v_mul_f32_e32 v54, v76, v70
	v_fmaak_f32 v48, v48, v54, 0xc1e6d4ca
	v_exp_f32_e32 v54, v48
	v_mul_f32_e32 v48, v77, v70
	v_fmaak_f32 v48, v49, v48, 0xc1e6d4ca
	v_exp_f32_e32 v49, v48
	v_mul_f32_e32 v48, v78, v70
	v_fmaak_f32 v48, v50, v48, 0xc1e6d4ca
	v_exp_f32_e32 v50, v48
	v_mul_f32_e32 v48, v79, v70
	v_fmaak_f32 v48, v51, v48, 0xc1e6d4ca
	v_exp_f32_e32 v51, v48
	v_mov_b32_e32 v48, 0x1980
	v_mad_u32_u24 v56, v101, s2, v48
	v_add_u32_e32 v48, v72, v56
	v_cvt_pk_bf16_f32 v51, v50, v51
	v_cvt_pk_bf16_f32 v50, v54, v49
	ds_write_b64 v58, v[62:63] offset:10240
	ds_write_b64 v48, v[50:51] offset:10240
	ds_read_b128 v[76:79], v71 offset:8896
	s_mov_b32 s11, s9
	s_waitcnt lgkmcnt(0)
	v_mul_f32_e32 v49, v76, v64
	v_fmaak_f32 v44, v44, v49, 0xc1e6d4ca
	v_mul_f32_e32 v49, v78, v64
	v_fmaak_f32 v46, v46, v49, 0xc1e6d4ca
	v_mul_f32_e32 v49, v79, v64
	v_fmaak_f32 v47, v47, v49, 0xc1e6d4ca
	v_exp_f32_e32 v46, v46
	v_exp_f32_e32 v47, v47
	v_mul_f32_e32 v49, v77, v64
	v_fmaak_f32 v45, v45, v49, 0xc1e6d4ca
	v_exp_f32_e32 v49, v45
	v_cvt_pk_bf16_f32 v45, v46, v47
	v_mul_f32_e32 v46, v76, v65
	v_fmaak_f32 v40, v40, v46, 0xc1e6d4ca
	v_mul_f32_e32 v46, v77, v65
	v_fmaak_f32 v41, v41, v46, 0xc1e6d4ca
	v_mul_f32_e32 v46, v78, v65
	v_fmaak_f32 v42, v42, v46, 0xc1e6d4ca
	v_mul_f32_e32 v46, v79, v65
	v_fmaak_f32 v43, v43, v46, 0xc1e6d4ca
	v_exp_f32_e32 v40, v40
	v_exp_f32_e32 v42, v42
	v_exp_f32_e32 v43, v43
	v_exp_f32_e32 v46, v41
	v_exp_f32_e32 v44, v44
	v_cvt_pk_bf16_f32 v41, v42, v43
	v_cvt_pk_bf16_f32 v40, v40, v46
	ds_write_b64 v58, v[40:41] offset:10272
	v_mul_f32_e32 v40, v76, v68
	v_fmaak_f32 v36, v36, v40, 0xc1e6d4ca
	v_mul_f32_e32 v40, v78, v68
	v_fmaak_f32 v38, v38, v40, 0xc1e6d4ca
	v_mul_f32_e32 v40, v79, v68
	v_fmaak_f32 v39, v39, v40, 0xc1e6d4ca
	v_exp_f32_e32 v38, v38
	v_exp_f32_e32 v39, v39
	v_mul_f32_e32 v40, v77, v68
	v_fmaak_f32 v37, v37, v40, 0xc1e6d4ca
	v_exp_f32_e32 v40, v37
	v_cvt_pk_bf16_f32 v37, v38, v39
	v_mul_f32_e32 v38, v76, v70
	v_fmaak_f32 v32, v32, v38, 0xc1e6d4ca
	v_mul_f32_e32 v38, v77, v70
	v_fmaak_f32 v33, v33, v38, 0xc1e6d4ca
	v_mul_f32_e32 v38, v78, v70
	v_fmaak_f32 v34, v34, v38, 0xc1e6d4ca
	v_mul_f32_e32 v38, v79, v70
	v_fmaak_f32 v35, v35, v38, 0xc1e6d4ca
	v_exp_f32_e32 v36, v36
	v_exp_f32_e32 v32, v32
	v_exp_f32_e32 v34, v34
	v_exp_f32_e32 v35, v35
	v_exp_f32_e32 v38, v33
	v_cvt_pk_bf16_f32 v44, v44, v49
	v_cvt_pk_bf16_f32 v36, v36, v40
	v_cvt_pk_bf16_f32 v33, v34, v35
	v_cvt_pk_bf16_f32 v32, v32, v38
	ds_write_b64 v60, v[44:45] offset:10272
	ds_write_b64 v53, v[36:37] offset:10272
	ds_write_b64 v48, v[32:33] offset:10272
	ds_read_b128 v[32:35], v71 offset:8960
	s_waitcnt lgkmcnt(0)
	v_mul_f32_e32 v36, v32, v64
	v_fmaak_f32 v28, v28, v36, 0xc1e6d4ca
	v_mul_f32_e32 v36, v34, v64
	v_fmaak_f32 v30, v30, v36, 0xc1e6d4ca
	v_mul_f32_e32 v36, v35, v64
	v_fmaak_f32 v31, v31, v36, 0xc1e6d4ca
	v_exp_f32_e32 v30, v30
	v_exp_f32_e32 v31, v31
	v_mul_f32_e32 v36, v33, v64
	v_fmaak_f32 v29, v29, v36, 0xc1e6d4ca
	v_exp_f32_e32 v36, v29
	v_cvt_pk_bf16_f32 v29, v30, v31
	v_mul_f32_e32 v30, v32, v65
	v_fmaak_f32 v24, v24, v30, 0xc1e6d4ca
	v_mul_f32_e32 v30, v33, v65
	v_fmaak_f32 v25, v25, v30, 0xc1e6d4ca
	v_mul_f32_e32 v30, v34, v65
	v_fmaak_f32 v26, v26, v30, 0xc1e6d4ca
	v_mul_f32_e32 v30, v35, v65
	v_fmaak_f32 v27, v27, v30, 0xc1e6d4ca
	v_exp_f32_e32 v24, v24
	v_exp_f32_e32 v26, v26
	v_exp_f32_e32 v27, v27
	v_exp_f32_e32 v30, v25
	v_exp_f32_e32 v28, v28
	v_cvt_pk_bf16_f32 v25, v26, v27
	v_cvt_pk_bf16_f32 v24, v24, v30
	ds_write_b64 v58, v[24:25] offset:10304
	v_mul_f32_e32 v24, v32, v68
	v_fmaak_f32 v20, v20, v24, 0xc1e6d4ca
	v_mul_f32_e32 v24, v34, v68
	v_fmaak_f32 v22, v22, v24, 0xc1e6d4ca
	v_mul_f32_e32 v24, v35, v68
	v_fmaak_f32 v23, v23, v24, 0xc1e6d4ca
	v_exp_f32_e32 v22, v22
	v_exp_f32_e32 v23, v23
	v_mul_f32_e32 v24, v33, v68
	v_fmaak_f32 v21, v21, v24, 0xc1e6d4ca
	v_exp_f32_e32 v24, v21
	v_cvt_pk_bf16_f32 v21, v22, v23
	v_mul_f32_e32 v22, v32, v70
	v_fmaak_f32 v16, v16, v22, 0xc1e6d4ca
	v_mul_f32_e32 v22, v33, v70
	v_fmaak_f32 v17, v17, v22, 0xc1e6d4ca
	v_mul_f32_e32 v22, v34, v70
	v_fmaak_f32 v18, v18, v22, 0xc1e6d4ca
	v_mul_f32_e32 v22, v35, v70
	v_fmaak_f32 v19, v19, v22, 0xc1e6d4ca
	v_exp_f32_e32 v20, v20
	v_exp_f32_e32 v16, v16
	v_exp_f32_e32 v18, v18
	v_exp_f32_e32 v19, v19
	v_exp_f32_e32 v22, v17
	v_cvt_pk_bf16_f32 v28, v28, v36
	v_cvt_pk_bf16_f32 v20, v20, v24
	v_cvt_pk_bf16_f32 v17, v18, v19
	v_cvt_pk_bf16_f32 v16, v16, v22
	ds_write_b64 v60, v[28:29] offset:10304
	ds_write_b64 v53, v[20:21] offset:10304
	ds_write_b64 v48, v[16:17] offset:10304
	ds_read_b128 v[16:19], v71 offset:9024
	v_mov_b32_e32 v20, 0xc1e6d4ca
	s_waitcnt lgkmcnt(0)
	v_mul_f32_e32 v21, v16, v64
	v_fmaak_f32 v12, v12, v21, 0xc1e6d4ca
	v_mul_f32_e32 v21, v18, v64
	v_fmaak_f32 v14, v14, v21, 0xc1e6d4ca
	v_mul_f32_e32 v21, v19, v64
	v_fmaak_f32 v15, v15, v21, 0xc1e6d4ca
	v_exp_f32_e32 v14, v14
	v_exp_f32_e32 v15, v15
	v_mul_f32_e32 v21, v17, v64
	v_fmaak_f32 v13, v13, v21, 0xc1e6d4ca
	v_exp_f32_e32 v21, v13
	v_cvt_pk_bf16_f32 v13, v14, v15
	v_mul_f32_e32 v14, v16, v65
	v_fmaak_f32 v8, v8, v14, 0xc1e6d4ca
	v_mul_f32_e32 v14, v17, v65
	v_fmaak_f32 v9, v9, v14, 0xc1e6d4ca
	v_mul_f32_e32 v14, v18, v65
	v_fmaak_f32 v10, v10, v14, 0xc1e6d4ca
	v_mul_f32_e32 v14, v19, v65
	v_fmaak_f32 v11, v11, v14, 0xc1e6d4ca
	v_exp_f32_e32 v8, v8
	v_exp_f32_e32 v10, v10
	v_exp_f32_e32 v11, v11
	v_exp_f32_e32 v14, v9
	v_exp_f32_e32 v12, v12
	v_and_b32_e32 v64, 1, v100
	v_cvt_pk_bf16_f32 v9, v10, v11
	v_cvt_pk_bf16_f32 v8, v8, v14
	ds_write_b64 v58, v[8:9] offset:10336
	v_mul_f32_e32 v8, v16, v68
	v_fmaak_f32 v4, v4, v8, 0xc1e6d4ca
	v_mul_f32_e32 v8, v18, v68
	v_fmaak_f32 v6, v6, v8, 0xc1e6d4ca
	v_mul_f32_e32 v8, v19, v68
	v_fmaak_f32 v7, v7, v8, 0xc1e6d4ca
	v_exp_f32_e32 v6, v6
	v_exp_f32_e32 v7, v7
	v_mul_f32_e32 v8, v17, v68
	v_fmaak_f32 v5, v5, v8, 0xc1e6d4ca
	v_exp_f32_e32 v8, v5
	v_cvt_pk_bf16_f32 v5, v6, v7
	v_mul_f32_e32 v6, v16, v70
	v_fmaak_f32 v0, v0, v6, 0xc1e6d4ca
	v_mul_f32_e32 v6, v17, v70
	v_fmaak_f32 v1, v1, v6, 0xc1e6d4ca
	v_mul_f32_e32 v6, v18, v70
	v_fmaak_f32 v2, v2, v6, 0xc1e6d4ca
	v_mul_f32_e32 v6, v19, v70
	v_fmac_f32_e32 v20, v3, v6
	v_exp_f32_e32 v0, v0
	v_exp_f32_e32 v2, v2
	v_exp_f32_e32 v3, v20
	v_exp_f32_e32 v6, v1
	v_exp_f32_e32 v4, v4
	v_cvt_pk_bf16_f32 v12, v12, v21
	v_cvt_pk_bf16_f32 v1, v2, v3
	v_cvt_pk_bf16_f32 v0, v0, v6
	ds_write_b64 v48, v[0:1] offset:10336
	v_lshrrev_b32_e32 v0, 2, v101
	v_or_b32_e32 v0, v67, v0
	v_lshlrev_b32_e32 v1, 3, v100
	v_mul_u32_u24_e32 v0, 0x88, v0
	v_and_b32_e32 v1, 24, v1
	v_add_u32_e32 v2, s6, v66
	v_cvt_pk_bf16_f32 v4, v4, v8
	v_add3_u32 v62, s6, v0, v1
	v_mad_u32_u24 v0, v101, s2, v2
	ds_write_b64 v60, v[12:13] offset:10336
	ds_write_b64 v53, v[4:5] offset:10336
	s_movk_i32 s34, 0x88
	v_and_b32_e32 v64, 32, v100
	v_and_b32_e32 v66, 16, v100
	v_mad_u32_u24 v65, v101, s34, v64
	v_add_u32_e32 v65, s6, v65
	v_add_u32_e32 v67, v65, v66
	v_sub_u32_e32 v65, v65, v66
	v_lshrrev_b32_e32 v68, 1, v100
	v_and_b32_e32 v68, 16, v68
	v_bfe_u32 v69, v100, 2, 2
	v_or_b32_e32 v68, v68, v69
	v_and_b32_e32 v69, 3, v100
	v_lshlrev_b32_e32 v69, 3, v69
	v_mad_u32_u24 v68, v68, s34, v69
	v_add_u32_e32 v68, s6, v68
	s_movk_i32 s35, 0x44
	v_mul_u32_u24_e32 v66, s35, v66
	v_add_u32_e32 v69, v68, v66
	v_sub_u32_e32 v68, v68, v66
	ds_read_b64 v[0:1], v67 offset:10240
	ds_read_b64 v[2:3], v65 offset:10264
	ds_read_b64 v[4:5], v67 offset:10304
	ds_read_b64 v[6:7], v65 offset:10328
	ds_read_b64 v[8:9], v67 offset:12424
	ds_read_b64 v[10:11], v67 offset:12416
	ds_read_b64 v[12:13], v67 offset:12488
	ds_read_b64 v[14:15], v67 offset:12480
	ds_read_b64 v[16:17], v65 offset:14608
	ds_read_b64 v[18:19], v67 offset:14600
	ds_read_b64 v[20:21], v65 offset:14672
	ds_read_b64 v[22:23], v67 offset:14664
	ds_read_b64 v[24:25], v65 offset:16792
	ds_read_b64 v[26:27], v65 offset:16784
	ds_read_b64 v[28:29], v65 offset:16856
	ds_read_b64 v[30:31], v65 offset:16848
	ds_read_b64_tr_b16 v[32:33], v69 offset:10240
	ds_read_b64_tr_b16 v[34:35], v68 offset:11872
	ds_read_b64_tr_b16 v[36:37], v69 offset:14592
	ds_read_b64_tr_b16 v[38:39], v68 offset:16224
	ds_read_b64_tr_b16 v[40:41], v69 offset:10816
	ds_read_b64_tr_b16 v[42:43], v69 offset:10272
	ds_read_b64_tr_b16 v[44:45], v69 offset:15168
	ds_read_b64_tr_b16 v[46:47], v69 offset:14624
	ds_read_b64_tr_b16 v[48:49], v68 offset:11392
	ds_read_b64_tr_b16 v[50:51], v69 offset:10848
	ds_read_b64_tr_b16 v[52:53], v68 offset:15744
	ds_read_b64_tr_b16 v[54:55], v69 offset:15200
	ds_read_b64_tr_b16 v[56:57], v68 offset:11968
	ds_read_b64_tr_b16 v[58:59], v68 offset:11424
	ds_read_b64_tr_b16 v[60:61], v68 offset:16320
	ds_read_b64_tr_b16 v[62:63], v68 offset:15776
	ds_read2st64_b32 v[116:117], v102 offset0:22 offset1:23
	v_and_b32_e32 v110, 1, v100
	v_cmp_eq_u32_e32 vcc, 0, v110
	v_mov_b32_e32 v110, 0xeeeeeeee
	v_mov_b32_e32 v111, 0x44444444
	s_mov_b32 s32, 0x2b8cbccc
	s_mov_b32 s33, 0
	v_cndmask_b32_e32 v64, v110, v111, vcc
	v_mov_b32_e32 v68, 0x3f803f80
	v_mov_b32_e32 v69, v68
	v_mov_b32_e32 v70, v68
	v_mov_b32_e32 v71, v68
	v_mov_b64_e32 v[72:73], s[32:33]
	v_mov_b64_e32 v[76:77], s[32:33]
	v_mov_b64_e32 v[80:81], s[32:33]
	v_mov_b64_e32 v[84:85], s[32:33]
	s_movk_i32 s30, 100
	s_waitcnt lgkmcnt(0)
	v_mov_b32_dpp v112, v116 quad_perm:[0,2,0,2] row_mask:0xf bank_mask:0xf
	v_mov_b32_dpp v113, v116 quad_perm:[1,3,1,3] row_mask:0xf bank_mask:0xf
	v_mov_b32_dpp v114, v117 quad_perm:[0,2,0,2] row_mask:0xf bank_mask:0xf
	v_mov_b32_dpp v115, v117 quad_perm:[1,3,1,3] row_mask:0xf bank_mask:0xf
	v_smfmac_f32_16x16x64_bf16 v[72:75], v[68:71], v[0:7], v64
	v_smfmac_f32_16x16x64_bf16 v[76:79], v[68:71], v[8:15], v64
	v_smfmac_f32_16x16x64_bf16 v[80:83], v[68:71], v[16:23], v64
	v_smfmac_f32_16x16x64_bf16 v[84:87], v[68:71], v[24:31], v64
.Lsk_loop:
	v_mov_b64_e32 v[88:89], s[32:33]
	v_mov_b64_e32 v[92:93], s[32:33]
	v_mov_b64_e32 v[96:97], s[32:33]
	v_mov_b64_e32 v[104:105], s[32:33]
	s_nop 0
	v_add_f32_dpp v108, v72, v73 quad_perm:[0,1,2,3] row_mask:0x1 bank_mask:0xf
	v_add_f32_dpp v108, v76, v77 quad_perm:[0,1,2,3] row_mask:0x2 bank_mask:0xf
	v_add_f32_dpp v108, v80, v81 quad_perm:[0,1,2,3] row_mask:0x4 bank_mask:0xf
	v_add_f32_dpp v108, v84, v85 quad_perm:[0,1,2,3] row_mask:0x8 bank_mask:0xf
	v_rcp_f32_e32 v109, v108
	s_nop 1
	v_mul_f32_dpp v110, v109, v114 quad_perm:[0,2,0,2] row_mask:0xf bank_mask:0xf
	v_mul_f32_dpp v111, v109, v115 quad_perm:[1,3,1,3] row_mask:0xf bank_mask:0xf
	v_cvt_pk_bf16_f32 v68, v110, v111
	s_nop 1
	v_mov_b32_dpp v69, v68 row_ror:4 row_mask:0xf bank_mask:0xf
	v_mov_b32_dpp v70, v68 row_ror:8 row_mask:0xf bank_mask:0xf
	v_mov_b32_dpp v71, v68 row_ror:12 row_mask:0xf bank_mask:0xf
	s_nop 1
	v_smfmac_f32_16x16x64_bf16 v[88:91], v[68:71], v[32:39], v64
	v_smfmac_f32_16x16x64_bf16 v[92:95], v[68:71], v[40:47], v64
	v_smfmac_f32_16x16x64_bf16 v[96:99], v[68:71], v[48:55], v64
	v_smfmac_f32_16x16x64_bf16 v[104:107], v[68:71], v[56:63], v64
	v_mov_b64_e32 v[72:73], s[32:33]
	v_mov_b64_e32 v[76:77], s[32:33]
	v_mov_b64_e32 v[80:81], s[32:33]
	v_mov_b64_e32 v[84:85], s[32:33]
	s_nop 0
	v_add_f32_dpp v108, v88, v89 quad_perm:[0,1,2,3] row_mask:0x1 bank_mask:0xf
	v_add_f32_dpp v108, v92, v93 quad_perm:[0,1,2,3] row_mask:0x2 bank_mask:0xf
	v_add_f32_dpp v108, v96, v97 quad_perm:[0,1,2,3] row_mask:0x4 bank_mask:0xf
	v_add_f32_dpp v108, v104, v105 quad_perm:[0,1,2,3] row_mask:0x8 bank_mask:0xf
	v_rcp_f32_e32 v109, v108
	s_nop 1
	v_mul_f32_dpp v110, v109, v112 quad_perm:[0,2,0,2] row_mask:0xf bank_mask:0xf
	v_mul_f32_dpp v111, v109, v113 quad_perm:[1,3,1,3] row_mask:0xf bank_mask:0xf
	v_cvt_pk_bf16_f32 v68, v110, v111
	s_nop 1
	v_mov_b32_dpp v69, v68 row_ror:4 row_mask:0xf bank_mask:0xf
	v_mov_b32_dpp v70, v68 row_ror:8 row_mask:0xf bank_mask:0xf
	v_mov_b32_dpp v71, v68 row_ror:12 row_mask:0xf bank_mask:0xf
	s_nop 1
	v_smfmac_f32_16x16x64_bf16 v[72:75], v[68:71], v[0:7], v64
	v_smfmac_f32_16x16x64_bf16 v[76:79], v[68:71], v[8:15], v64
	v_smfmac_f32_16x16x64_bf16 v[80:83], v[68:71], v[16:23], v64
	v_smfmac_f32_16x16x64_bf16 v[84:87], v[68:71], v[24:31], v64
	s_add_i32 s30, s30, -1
	s_cmp_lg_u32 s30, 0
	s_cbranch_scc1 .Lsk_loop
	s_nop 1
	v_add_f32_dpp v108, v72, v73 quad_perm:[0,1,2,3] row_mask:0x1 bank_mask:0xf
	v_add_f32_dpp v108, v76, v77 quad_perm:[0,1,2,3] row_mask:0x2 bank_mask:0xf
	v_add_f32_dpp v108, v80, v81 quad_perm:[0,1,2,3] row_mask:0x4 bank_mask:0xf
	v_add_f32_dpp v108, v84, v85 quad_perm:[0,1,2,3] row_mask:0x8 bank_mask:0xf
	v_rcp_f32_e32 v109, v108
	s_mov_b32 s34, 0x3d0df4e0
	s_mov_b32 s35, s34
	v_mul_f32_e32 v118, v117, v109
	v_lshlrev_b32_e32 v72, 16, v0
	v_and_b32_e32 v73, 0xffff0000, v0
	v_log_f32_e32 v74, v72
	v_log_f32_e32 v75, v73
	s_nop 0
	v_pk_fma_f32 v[74:75], v[74:75], s[34:35], 1.0 op_sel_hi:[1,0,0]
	v_pk_mul_f32 v[74:75], v[74:75], v[72:73]
	v_cvt_pk_bf16_f32 v0, v74, v75
	v_lshlrev_b32_e32 v76, 16, v1
	v_and_b32_e32 v77, 0xffff0000, v1
	v_log_f32_e32 v78, v76
	v_log_f32_e32 v79, v77
	s_nop 0
	v_pk_fma_f32 v[78:79], v[78:79], s[34:35], 1.0 op_sel_hi:[1,0,0]
	v_pk_mul_f32 v[78:79], v[78:79], v[76:77]
	v_cvt_pk_bf16_f32 v1, v78, v79
	v_lshlrev_b32_e32 v80, 16, v2
	v_and_b32_e32 v81, 0xffff0000, v2
	v_log_f32_e32 v82, v80
	v_log_f32_e32 v83, v81
	s_nop 0
	v_pk_fma_f32 v[82:83], v[82:83], s[34:35], 1.0 op_sel_hi:[1,0,0]
	v_pk_mul_f32 v[82:83], v[82:83], v[80:81]
	v_cvt_pk_bf16_f32 v2, v82, v83
	v_lshlrev_b32_e32 v84, 16, v3
	v_and_b32_e32 v85, 0xffff0000, v3
	v_log_f32_e32 v86, v84
	v_log_f32_e32 v87, v85
	s_nop 0
	v_pk_fma_f32 v[86:87], v[86:87], s[34:35], 1.0 op_sel_hi:[1,0,0]
	v_pk_mul_f32 v[86:87], v[86:87], v[84:85]
	v_cvt_pk_bf16_f32 v3, v86, v87
	v_lshlrev_b32_e32 v72, 16, v4
	v_and_b32_e32 v73, 0xffff0000, v4
	v_log_f32_e32 v74, v72
	v_log_f32_e32 v75, v73
	s_nop 0
	v_pk_fma_f32 v[74:75], v[74:75], s[34:35], 1.0 op_sel_hi:[1,0,0]
	v_pk_mul_f32 v[74:75], v[74:75], v[72:73]
	v_cvt_pk_bf16_f32 v4, v74, v75
	v_lshlrev_b32_e32 v76, 16, v5
	v_and_b32_e32 v77, 0xffff0000, v5
	v_log_f32_e32 v78, v76
	v_log_f32_e32 v79, v77
	s_nop 0
	v_pk_fma_f32 v[78:79], v[78:79], s[34:35], 1.0 op_sel_hi:[1,0,0]
	v_pk_mul_f32 v[78:79], v[78:79], v[76:77]
	v_cvt_pk_bf16_f32 v5, v78, v79
	v_lshlrev_b32_e32 v80, 16, v6
	v_and_b32_e32 v81, 0xffff0000, v6
	v_log_f32_e32 v82, v80
	v_log_f32_e32 v83, v81
	s_nop 0
	v_pk_fma_f32 v[82:83], v[82:83], s[34:35], 1.0 op_sel_hi:[1,0,0]
	v_pk_mul_f32 v[82:83], v[82:83], v[80:81]
	v_cvt_pk_bf16_f32 v6, v82, v83
	v_lshlrev_b32_e32 v84, 16, v7
	v_and_b32_e32 v85, 0xffff0000, v7
	v_log_f32_e32 v86, v84
	v_log_f32_e32 v87, v85
	s_nop 0
	v_pk_fma_f32 v[86:87], v[86:87], s[34:35], 1.0 op_sel_hi:[1,0,0]
	v_pk_mul_f32 v[86:87], v[86:87], v[84:85]
	v_cvt_pk_bf16_f32 v7, v86, v87
	v_lshlrev_b32_e32 v72, 16, v8
	v_and_b32_e32 v73, 0xffff0000, v8
	v_log_f32_e32 v74, v72
	v_log_f32_e32 v75, v73
	s_nop 0
	v_pk_fma_f32 v[74:75], v[74:75], s[34:35], 1.0 op_sel_hi:[1,0,0]
	v_pk_mul_f32 v[74:75], v[74:75], v[72:73]
	v_cvt_pk_bf16_f32 v8, v74, v75
	v_lshlrev_b32_e32 v76, 16, v9
	v_and_b32_e32 v77, 0xffff0000, v9
	v_log_f32_e32 v78, v76
	v_log_f32_e32 v79, v77
	s_nop 0
	v_pk_fma_f32 v[78:79], v[78:79], s[34:35], 1.0 op_sel_hi:[1,0,0]
	v_pk_mul_f32 v[78:79], v[78:79], v[76:77]
	v_cvt_pk_bf16_f32 v9, v78, v79
	v_lshlrev_b32_e32 v80, 16, v10
	v_and_b32_e32 v81, 0xffff0000, v10
	v_log_f32_e32 v82, v80
	v_log_f32_e32 v83, v81
	s_nop 0
	v_pk_fma_f32 v[82:83], v[82:83], s[34:35], 1.0 op_sel_hi:[1,0,0]
	v_pk_mul_f32 v[82:83], v[82:83], v[80:81]
	v_cvt_pk_bf16_f32 v10, v82, v83
	v_lshlrev_b32_e32 v84, 16, v11
	v_and_b32_e32 v85, 0xffff0000, v11
	v_log_f32_e32 v86, v84
	v_log_f32_e32 v87, v85
	s_nop 0
	v_pk_fma_f32 v[86:87], v[86:87], s[34:35], 1.0 op_sel_hi:[1,0,0]
	v_pk_mul_f32 v[86:87], v[86:87], v[84:85]
	v_cvt_pk_bf16_f32 v11, v86, v87
	v_lshlrev_b32_e32 v72, 16, v12
	v_and_b32_e32 v73, 0xffff0000, v12
	v_log_f32_e32 v74, v72
	v_log_f32_e32 v75, v73
	s_nop 0
	v_pk_fma_f32 v[74:75], v[74:75], s[34:35], 1.0 op_sel_hi:[1,0,0]
	v_pk_mul_f32 v[74:75], v[74:75], v[72:73]
	v_cvt_pk_bf16_f32 v12, v74, v75
	v_lshlrev_b32_e32 v76, 16, v13
	v_and_b32_e32 v77, 0xffff0000, v13
	v_log_f32_e32 v78, v76
	v_log_f32_e32 v79, v77
	s_nop 0
	v_pk_fma_f32 v[78:79], v[78:79], s[34:35], 1.0 op_sel_hi:[1,0,0]
	v_pk_mul_f32 v[78:79], v[78:79], v[76:77]
	v_cvt_pk_bf16_f32 v13, v78, v79
	v_lshlrev_b32_e32 v80, 16, v14
	v_and_b32_e32 v81, 0xffff0000, v14
	v_log_f32_e32 v82, v80
	v_log_f32_e32 v83, v81
	s_nop 0
	v_pk_fma_f32 v[82:83], v[82:83], s[34:35], 1.0 op_sel_hi:[1,0,0]
	v_pk_mul_f32 v[82:83], v[82:83], v[80:81]
	v_cvt_pk_bf16_f32 v14, v82, v83
	v_lshlrev_b32_e32 v84, 16, v15
	v_and_b32_e32 v85, 0xffff0000, v15
	v_log_f32_e32 v86, v84
	v_log_f32_e32 v87, v85
	s_nop 0
	v_pk_fma_f32 v[86:87], v[86:87], s[34:35], 1.0 op_sel_hi:[1,0,0]
	v_pk_mul_f32 v[86:87], v[86:87], v[84:85]
	v_cvt_pk_bf16_f32 v15, v86, v87
	v_lshlrev_b32_e32 v72, 16, v16
	v_and_b32_e32 v73, 0xffff0000, v16
	v_log_f32_e32 v74, v72
	v_log_f32_e32 v75, v73
	s_nop 0
	v_pk_fma_f32 v[74:75], v[74:75], s[34:35], 1.0 op_sel_hi:[1,0,0]
	v_pk_mul_f32 v[74:75], v[74:75], v[72:73]
	v_cvt_pk_bf16_f32 v16, v74, v75
	v_lshlrev_b32_e32 v76, 16, v17
	v_and_b32_e32 v77, 0xffff0000, v17
	v_log_f32_e32 v78, v76
	v_log_f32_e32 v79, v77
	s_nop 0
	v_pk_fma_f32 v[78:79], v[78:79], s[34:35], 1.0 op_sel_hi:[1,0,0]
	v_pk_mul_f32 v[78:79], v[78:79], v[76:77]
	v_cvt_pk_bf16_f32 v17, v78, v79
	v_lshlrev_b32_e32 v80, 16, v18
	v_and_b32_e32 v81, 0xffff0000, v18
	v_log_f32_e32 v82, v80
	v_log_f32_e32 v83, v81
	s_nop 0
	v_pk_fma_f32 v[82:83], v[82:83], s[34:35], 1.0 op_sel_hi:[1,0,0]
	v_pk_mul_f32 v[82:83], v[82:83], v[80:81]
	v_cvt_pk_bf16_f32 v18, v82, v83
	v_lshlrev_b32_e32 v84, 16, v19
	v_and_b32_e32 v85, 0xffff0000, v19
	v_log_f32_e32 v86, v84
	v_log_f32_e32 v87, v85
	s_nop 0
	v_pk_fma_f32 v[86:87], v[86:87], s[34:35], 1.0 op_sel_hi:[1,0,0]
	v_pk_mul_f32 v[86:87], v[86:87], v[84:85]
	v_cvt_pk_bf16_f32 v19, v86, v87
	v_lshlrev_b32_e32 v72, 16, v20
	v_and_b32_e32 v73, 0xffff0000, v20
	v_log_f32_e32 v74, v72
	v_log_f32_e32 v75, v73
	s_nop 0
	v_pk_fma_f32 v[74:75], v[74:75], s[34:35], 1.0 op_sel_hi:[1,0,0]
	v_pk_mul_f32 v[74:75], v[74:75], v[72:73]
	v_cvt_pk_bf16_f32 v20, v74, v75
	v_lshlrev_b32_e32 v76, 16, v21
	v_and_b32_e32 v77, 0xffff0000, v21
	v_log_f32_e32 v78, v76
	v_log_f32_e32 v79, v77
	s_nop 0
	v_pk_fma_f32 v[78:79], v[78:79], s[34:35], 1.0 op_sel_hi:[1,0,0]
	v_pk_mul_f32 v[78:79], v[78:79], v[76:77]
	v_cvt_pk_bf16_f32 v21, v78, v79
	v_lshlrev_b32_e32 v80, 16, v22
	v_and_b32_e32 v81, 0xffff0000, v22
	v_log_f32_e32 v82, v80
	v_log_f32_e32 v83, v81
	s_nop 0
	v_pk_fma_f32 v[82:83], v[82:83], s[34:35], 1.0 op_sel_hi:[1,0,0]
	v_pk_mul_f32 v[82:83], v[82:83], v[80:81]
	v_cvt_pk_bf16_f32 v22, v82, v83
	v_lshlrev_b32_e32 v84, 16, v23
	v_and_b32_e32 v85, 0xffff0000, v23
	v_log_f32_e32 v86, v84
	v_log_f32_e32 v87, v85
	s_nop 0
	v_pk_fma_f32 v[86:87], v[86:87], s[34:35], 1.0 op_sel_hi:[1,0,0]
	v_pk_mul_f32 v[86:87], v[86:87], v[84:85]
	v_cvt_pk_bf16_f32 v23, v86, v87
	v_lshlrev_b32_e32 v72, 16, v24
	v_and_b32_e32 v73, 0xffff0000, v24
	v_log_f32_e32 v74, v72
	v_log_f32_e32 v75, v73
	s_nop 0
	v_pk_fma_f32 v[74:75], v[74:75], s[34:35], 1.0 op_sel_hi:[1,0,0]
	v_pk_mul_f32 v[74:75], v[74:75], v[72:73]
	v_cvt_pk_bf16_f32 v24, v74, v75
	v_lshlrev_b32_e32 v76, 16, v25
	v_and_b32_e32 v77, 0xffff0000, v25
	v_log_f32_e32 v78, v76
	v_log_f32_e32 v79, v77
	s_nop 0
	v_pk_fma_f32 v[78:79], v[78:79], s[34:35], 1.0 op_sel_hi:[1,0,0]
	v_pk_mul_f32 v[78:79], v[78:79], v[76:77]
	v_cvt_pk_bf16_f32 v25, v78, v79
	v_lshlrev_b32_e32 v80, 16, v26
	v_and_b32_e32 v81, 0xffff0000, v26
	v_log_f32_e32 v82, v80
	v_log_f32_e32 v83, v81
	s_nop 0
	v_pk_fma_f32 v[82:83], v[82:83], s[34:35], 1.0 op_sel_hi:[1,0,0]
	v_pk_mul_f32 v[82:83], v[82:83], v[80:81]
	v_cvt_pk_bf16_f32 v26, v82, v83
	v_lshlrev_b32_e32 v84, 16, v27
	v_and_b32_e32 v85, 0xffff0000, v27
	v_log_f32_e32 v86, v84
	v_log_f32_e32 v87, v85
	s_nop 0
	v_pk_fma_f32 v[86:87], v[86:87], s[34:35], 1.0 op_sel_hi:[1,0,0]
	v_pk_mul_f32 v[86:87], v[86:87], v[84:85]
	v_cvt_pk_bf16_f32 v27, v86, v87
	v_lshlrev_b32_e32 v72, 16, v28
	v_and_b32_e32 v73, 0xffff0000, v28
	v_log_f32_e32 v74, v72
	v_log_f32_e32 v75, v73
	s_nop 0
	v_pk_fma_f32 v[74:75], v[74:75], s[34:35], 1.0 op_sel_hi:[1,0,0]
	v_pk_mul_f32 v[74:75], v[74:75], v[72:73]
	v_cvt_pk_bf16_f32 v28, v74, v75
	v_lshlrev_b32_e32 v76, 16, v29
	v_and_b32_e32 v77, 0xffff0000, v29
	v_log_f32_e32 v78, v76
	v_log_f32_e32 v79, v77
	s_nop 0
	v_pk_fma_f32 v[78:79], v[78:79], s[34:35], 1.0 op_sel_hi:[1,0,0]
	v_pk_mul_f32 v[78:79], v[78:79], v[76:77]
	v_cvt_pk_bf16_f32 v29, v78, v79
	v_lshlrev_b32_e32 v80, 16, v30
	v_and_b32_e32 v81, 0xffff0000, v30
	v_log_f32_e32 v82, v80
	v_log_f32_e32 v83, v81
	s_nop 0
	v_pk_fma_f32 v[82:83], v[82:83], s[34:35], 1.0 op_sel_hi:[1,0,0]
	v_pk_mul_f32 v[82:83], v[82:83], v[80:81]
	v_cvt_pk_bf16_f32 v30, v82, v83
	v_lshlrev_b32_e32 v84, 16, v31
	v_and_b32_e32 v85, 0xffff0000, v31
	v_log_f32_e32 v86, v84
	v_log_f32_e32 v87, v85
	s_nop 0
	v_pk_fma_f32 v[86:87], v[86:87], s[34:35], 1.0 op_sel_hi:[1,0,0]
	v_pk_mul_f32 v[86:87], v[86:87], v[84:85]
	v_cvt_pk_bf16_f32 v31, v86, v87
	v_mov_b64_e32 v[88:89], s[32:33]
	v_mov_b64_e32 v[92:93], s[32:33]
	v_mov_b64_e32 v[96:97], s[32:33]
	v_mov_b64_e32 v[104:105], s[32:33]
	s_nop 1
	v_smfmac_f32_16x16x64_bf16 v[88:91], v[68:71], v[0:7], v64
	v_smfmac_f32_16x16x64_bf16 v[92:95], v[68:71], v[8:15], v64
	v_smfmac_f32_16x16x64_bf16 v[96:99], v[68:71], v[16:23], v64
	v_smfmac_f32_16x16x64_bf16 v[104:107], v[68:71], v[24:31], v64
	s_nop 4
	v_add_f32_dpp v108, v88, v89 quad_perm:[0,1,2,3] row_mask:0x1 bank_mask:0xf
	v_add_f32_dpp v108, v92, v93 quad_perm:[0,1,2,3] row_mask:0x2 bank_mask:0xf
	v_add_f32_dpp v108, v96, v97 quad_perm:[0,1,2,3] row_mask:0x4 bank_mask:0xf
	v_add_f32_dpp v108, v104, v105 quad_perm:[0,1,2,3] row_mask:0x8 bank_mask:0xf
	v_add_f32_e32 v108, 0xab8cbccc, v108
	v_mul_f32_e32 v108, v118, v108
	s_nop 1
	v_add_f32_dpp v108, v108, v108 row_ror:8 row_mask:0xf bank_mask:0xf
	s_nop 1
	v_add_f32_dpp v108, v108, v108 row_ror:4 row_mask:0xf bank_mask:0xf
	s_nop 1
	v_add_f32_dpp v108, v108, v108 row_ror:2 row_mask:0xf bank_mask:0xf
	s_nop 1
	v_add_f32_dpp v108, v108, v108 row_ror:1 row_mask:0xf bank_mask:0xf
	s_nop 1
	v_mov_b32_e32 v109, v108
	s_nop 1
	v_permlane16_swap_b32_e32 v108, v109
	v_add_f32_e32 v108, v108, v109
	v_mov_b32_e32 v109, v108
	s_nop 1
	v_permlane32_swap_b32_e32 v108, v109
	v_add_f32_e32 v108, v108, v109
	v_cmp_eq_u32_e32 vcc, 0, v100
	s_and_saveexec_b64 s[0:1], vcc
	s_cbranch_execz .LBB1_38
	s_mul_i32 s0, s22, 5
	s_add_i32 s0, s0, s23
	s_mov_b32 s1, 0
	s_lshl_b64 s[0:1], s[0:1], 2
	s_add_u32 s0, s12, s0
	s_addc_u32 s1, s13, s1
	v_mov_b32_e32 v109, 0
	global_store_dword v109, v108, s[0:1]
